# retention epilogue parks O accumulators in LDS straight from AGPRs (no accvgpr_read)
# baseline (speedup 1.0000x reference)
.LBB1_26:
	v_lshlrev_b32_e32 v0, 4, v141
	s_or_b32 s0, s33, s71
	v_add3_u32 v0, v140, v0, s0
	v_mov_b32_e32 v1, 0
	v_lshlrev_b64 v[8:9], 11, v[0:1]
	v_or_b32_e32 v0, s70, v8
	v_lshl_or_b32 v8, v156, 2, v0
	v_lshlrev_b64 v[60:61], 1, v[8:9]
	v_lshl_add_u64 v[30:31], s[42:43], 0, v[60:61]
	s_movk_i32 s18, 0x2000
	v_add_co_u32_e32 v34, vcc, s18, v30
	s_movk_i32 s17, 0x4000
	s_nop 0
	v_addc_co_u32_e32 v35, vcc, 0, v31, vcc
	s_lshl_b32 s2, s70, 2
	v_add_co_u32_e32 v8, vcc, s17, v30
	s_waitcnt lgkmcnt(0)
	s_add_u32 s0, s44, s2
	v_addc_co_u32_e32 v9, vcc, 0, v31, vcc
	s_movk_i32 s16, 0x6000
	s_addc_u32 s1, s45, 0
	v_add_co_u32_e32 v10, vcc, s16, v30
	v_lshlrev_b32_e32 v38, 4, v156
	s_add_u32 s2, s46, s2
	v_addc_co_u32_e32 v11, vcc, 0, v31, vcc
	s_mov_b32 s15, 0x8000
	s_addc_u32 s3, s47, 0
	global_load_dwordx4 v[0:3], v38, s[0:1]
	global_load_dwordx4 v[4:7], v38, s[2:3]
	global_load_dwordx2 v[42:43], v[8:9], off offset:-4096
	global_load_dwordx2 v[32:33], v[8:9], off
	global_load_dwordx2 v[28:29], v[10:11], off offset:-4096
	global_load_dwordx2 v[26:27], v[10:11], off
	v_add_co_u32_e32 v8, vcc, s15, v30
	s_mov_b32 s14, 0xa000
	s_nop 0
	v_addc_co_u32_e32 v9, vcc, 0, v31, vcc
	v_add_co_u32_e32 v10, vcc, s14, v30
	s_mov_b32 s13, 0xc000
	s_nop 0
	v_addc_co_u32_e32 v11, vcc, 0, v31, vcc
	global_load_dwordx2 v[24:25], v[8:9], off offset:-4096
	global_load_dwordx2 v[22:23], v[8:9], off
	global_load_dwordx2 v[20:21], v[10:11], off offset:-4096
	global_load_dwordx2 v[18:19], v[10:11], off
	v_add_co_u32_e32 v8, vcc, s13, v30
	s_mov_b32 s12, 0xe000
	s_nop 0
	v_addc_co_u32_e32 v9, vcc, 0, v31, vcc
	v_add_co_u32_e32 v36, vcc, s12, v30
	s_mov_b32 s0, 0xf000
	s_nop 0
	v_addc_co_u32_e32 v37, vcc, 0, v31, vcc
	global_load_dwordx2 v[16:17], v[8:9], off offset:-4096
	global_load_dwordx2 v[14:15], v[8:9], off
	global_load_dwordx2 v[12:13], v[36:37], off offset:-4096
	global_load_dwordx2 v[10:11], v[36:37], off
	v_add_co_u32_e32 v36, vcc, s0, v30
	v_lshl_add_u32 v107, v137, 15, 0
	s_nop 0
	v_addc_co_u32_e32 v37, vcc, 0, v31, vcc
	v_lshlrev_b32_e32 v108, 2, v138
	global_load_dwordx2 v[96:97], v[30:31], off
	global_load_dwordx2 v[70:71], v[34:35], off offset:-4096
	global_load_dwordx2 v[68:69], v[34:35], off
	global_load_dwordx2 v[8:9], v[36:37], off
	s_nop 15
	s_nop 15
	s_nop 7
	v_add3_u32 v107, v107, v139, v108
	s_mov_b32 s28, 0x3727c5ac
	v_lshl_add_u64 v[60:61], s[48:49], 0, v[60:61]
	s_nop 0
	s_nop 0
	s_nop 0
	s_nop 0
	s_waitcnt vmcnt(0)
	s_barrier
	ds_write2_b32 v107, a0, a16 offset1:32
	v_add_u32_e32 v30, 0x400, v107
	ds_write2_b32 v30, a1, a17 offset1:32
	v_add_u32_e32 v31, 0x800, v107
	ds_write2_b32 v31, a2, a18 offset1:32
	v_add_u32_e32 v34, 0xc00, v107
	ds_write2_b32 v34, a3, a19 offset1:32
	v_add_u32_e32 v35, 0x2000, v107
	ds_write2_b32 v35, a4, a20 offset1:32
	v_add_u32_e32 v36, 0x2400, v107
	ds_write2_b32 v36, a5, a21 offset1:32
	v_add_u32_e32 v37, 0x2800, v107
	ds_write2_b32 v37, a6, a22 offset1:32
	v_add_u32_e32 v39, 0x2c00, v107
	ds_write2_b32 v39, a7, a23 offset1:32
	v_add_u32_e32 v40, 0x4000, v107
	ds_write2_b32 v40, a8, a24 offset1:32
	v_add_u32_e32 v41, 0x4400, v107
	ds_write2_b32 v41, a9, a25 offset1:32
	v_add_u32_e32 v44, 0x4800, v107
	ds_write2_b32 v44, a10, a26 offset1:32
	v_add_u32_e32 v45, 0x4c00, v107
	ds_write2_b32 v45, a11, a27 offset1:32
	v_add_u32_e32 v46, 0x6000, v107
	ds_write2_b32 v46, a12, a28 offset1:32
	v_add_u32_e32 v47, 0x6400, v107
	ds_write2_b32 v47, a13, a29 offset1:32
	v_add_u32_e32 v48, 0x6800, v107
	ds_write2_b32 v48, a14, a30 offset1:32
	v_add_u32_e32 v49, 0x6c00, v107
	ds_write2_b32 v49, a15, a31 offset1:32
	ds_write2_b32 v107, a32, a48 offset0:64 offset1:96
	ds_write2_b32 v30, a33, a49 offset0:64 offset1:96
	ds_write2_b32 v31, a34, a50 offset0:64 offset1:96
	ds_write2_b32 v34, a35, a51 offset0:64 offset1:96
	ds_write2_b32 v35, a36, a52 offset0:64 offset1:96
	ds_write2_b32 v36, a37, a53 offset0:64 offset1:96
	ds_write2_b32 v37, a38, a54 offset0:64 offset1:96
	ds_write2_b32 v39, a39, a55 offset0:64 offset1:96
	ds_write2_b32 v40, a40, a56 offset0:64 offset1:96
	ds_write2_b32 v41, a41, a57 offset0:64 offset1:96
	ds_write2_b32 v44, a42, a58 offset0:64 offset1:96
	ds_write2_b32 v45, a43, a59 offset0:64 offset1:96
	ds_write2_b32 v46, a44, a60 offset0:64 offset1:96
	ds_write2_b32 v47, a45, a61 offset0:64 offset1:96
	ds_write2_b32 v48, a46, a62 offset0:64 offset1:96
	ds_write2_b32 v49, a47, a63 offset0:64 offset1:96
	ds_write2_b32 v107, a64, a80 offset0:128 offset1:160
	ds_write2_b32 v30, a65, a81 offset0:128 offset1:160
	ds_write2_b32 v31, a66, a82 offset0:128 offset1:160
	ds_write2_b32 v34, a67, a83 offset0:128 offset1:160
	ds_write2_b32 v35, a68, a84 offset0:128 offset1:160
	ds_write2_b32 v36, a69, a85 offset0:128 offset1:160
	ds_write2_b32 v37, a70, a86 offset0:128 offset1:160
	ds_write2_b32 v39, a71, a87 offset0:128 offset1:160
	ds_write2_b32 v40, a72, a88 offset0:128 offset1:160
	ds_write2_b32 v41, a73, a89 offset0:128 offset1:160
	ds_write2_b32 v44, a74, a90 offset0:128 offset1:160
	ds_write2_b32 v45, a75, a91 offset0:128 offset1:160
	ds_write2_b32 v46, a76, a92 offset0:128 offset1:160
	ds_write2_b32 v47, a77, a93 offset0:128 offset1:160
	ds_write2_b32 v48, a78, a94 offset0:128 offset1:160
	ds_write2_b32 v49, a79, a95 offset0:128 offset1:160
	ds_write2_b32 v107, a96, a112 offset0:192 offset1:224
	ds_write2_b32 v30, a97, a113 offset0:192 offset1:224
	ds_write2_b32 v31, a98, a114 offset0:192 offset1:224
	ds_write2_b32 v34, a99, a115 offset0:192 offset1:224
	ds_write2_b32 v35, a100, a116 offset0:192 offset1:224
	ds_write2_b32 v36, a101, a117 offset0:192 offset1:224
	ds_write2_b32 v37, a102, a118 offset0:192 offset1:224
	ds_write2_b32 v39, a103, a119 offset0:192 offset1:224
	ds_write2_b32 v40, a104, a120 offset0:192 offset1:224
	ds_write2_b32 v41, a105, a121 offset0:192 offset1:224
	ds_write2_b32 v44, a106, a122 offset0:192 offset1:224
	ds_write2_b32 v45, a107, a123 offset0:192 offset1:224
	ds_write2_b32 v46, a108, a124 offset0:192 offset1:224
	ds_write2_b32 v47, a109, a125 offset0:192 offset1:224
	ds_write2_b32 v48, a110, a126 offset0:192 offset1:224
	ds_write2_b32 v49, a111, a127 offset0:192 offset1:224
	v_lshl_add_u32 v30, v136, 15, 0
	v_add3_u32 v116, v30, v143, v38
	v_add_u32_e32 v30, 0x10000, v116
	s_waitcnt lgkmcnt(0)
	s_barrier
	ds_read_b128 v[34:37], v30
	ds_read_b128 v[38:41], v116
	ds_read_b128 v[44:47], v116 offset:1024
	v_add_u32_e32 v30, 0x10400, v116
	ds_read_b128 v[48:51], v30
	s_waitcnt lgkmcnt(2)
	v_pk_add_f32 v[102:103], v[40:41], v[36:37]
	v_pk_add_f32 v[104:105], v[38:39], v[34:35]
	v_add_u32_e32 v38, 0x10800, v116
	v_mov_b32_e32 v34, v104
	v_mov_b32_e32 v35, v103
	ds_read_b128 v[38:41], v38
	v_pk_mov_b32 v[30:31], v[104:105], v[102:103] op_sel:[1,0]
	s_waitcnt lgkmcnt(1)
	v_pk_add_f32 v[98:99], v[46:47], v[50:51]
	v_pk_add_f32 v[132:133], v[30:31], v[34:35]
	v_pk_add_f32 v[100:101], v[44:45], v[48:49]
	ds_read_b128 v[34:37], v116 offset:2048
	v_pk_mov_b32 v[30:31], v[100:101], v[98:99] op_sel:[1,0]
	v_mov_b32_e32 v44, v100
	v_mov_b32_e32 v45, v99
	v_pk_add_f32 v[122:123], v[30:31], v[44:45]
	v_add_u32_e32 v30, 0x10c00, v116
	ds_read_b128 v[44:47], v116 offset:3072
	ds_read_b128 v[48:51], v30
	s_waitcnt lgkmcnt(2)
	v_pk_add_f32 v[92:93], v[36:37], v[40:41]
	v_pk_add_f32 v[94:95], v[34:35], v[38:39]
	v_mov_b32_e32 v35, v93
	v_pk_mov_b32 v[30:31], v[94:95], v[92:93] op_sel:[1,0]
	v_mov_b32_e32 v34, v94
	v_pk_add_f32 v[118:119], v[30:31], v[34:35]
	v_add_u32_e32 v34, 0x11000, v116
	s_waitcnt lgkmcnt(0)
	v_pk_add_f32 v[88:89], v[46:47], v[50:51]
	v_pk_add_f32 v[90:91], v[44:45], v[48:49]
	ds_read_b128 v[34:37], v34
	ds_read_b128 v[38:41], v116 offset:4096
	ds_read_b128 v[44:47], v116 offset:5120
	v_pk_mov_b32 v[30:31], v[90:91], v[88:89] op_sel:[1,0]
	v_mov_b32_e32 v52, v90
	v_add_u32_e32 v48, 0x11400, v116
	v_mov_b32_e32 v53, v89
	ds_read_b128 v[48:51], v48
	v_pk_add_f32 v[120:121], v[30:31], v[52:53]
	v_add_u32_e32 v30, 0x11800, v116
	s_waitcnt lgkmcnt(2)
	v_pk_add_f32 v[84:85], v[40:41], v[36:37]
	v_pk_add_f32 v[86:87], v[38:39], v[34:35]
	ds_read_b128 v[34:37], v116 offset:6144
	ds_read_b128 v[38:41], v30
	v_add_u32_e32 v30, 0x11c00, v116
	s_waitcnt lgkmcnt(2)
	v_pk_add_f32 v[80:81], v[46:47], v[50:51]
	v_pk_add_f32 v[82:83], v[44:45], v[48:49]
	ds_read_b128 v[48:51], v30
	v_add_u32_e32 v30, 0x12000, v116
	ds_read_b128 v[44:47], v116 offset:7168
	s_waitcnt lgkmcnt(2)
	v_pk_add_f32 v[74:75], v[36:37], v[40:41]
	v_pk_add_f32 v[76:77], v[34:35], v[38:39]
	ds_read_b128 v[34:37], v30
	ds_read_b128 v[38:41], v116 offset:8192
	ds_read_b128 v[52:55], v116 offset:9216
	v_add_u32_e32 v30, 0x12400, v116
	ds_read_b128 v[56:59], v30
	s_waitcnt lgkmcnt(4)
	v_pk_add_f32 v[72:73], v[46:47], v[50:51]
	s_waitcnt lgkmcnt(2)
	v_pk_add_f32 v[64:65], v[40:41], v[36:37]
	v_pk_add_f32 v[66:67], v[38:39], v[34:35]
	ds_read_b128 v[34:37], v116 offset:10240
	v_add_u32_e32 v30, 0x12800, v116
	ds_read_b128 v[38:41], v30
	v_pk_add_f32 v[78:79], v[44:45], v[48:49]
	ds_read_b128 v[44:47], v116 offset:11264
	v_add_u32_e32 v30, 0x12c00, v116
	ds_read_b128 v[48:51], v30
	v_add_u32_e32 v30, 0x13000, v116
	s_waitcnt lgkmcnt(4)
	v_pk_add_f32 v[58:59], v[54:55], v[58:59]
	v_pk_add_f32 v[62:63], v[52:53], v[56:57]
	s_waitcnt lgkmcnt(2)
	v_pk_add_f32 v[52:53], v[36:37], v[40:41]
	v_pk_add_f32 v[54:55], v[34:35], v[38:39]
	ds_read_b128 v[34:37], v30
	ds_read_b128 v[38:41], v116 offset:12288
	ds_read_b128 v[106:109], v116 offset:13312
	v_add_u32_e32 v30, 0x13400, v116
	ds_read_b128 v[110:113], v30
	s_waitcnt lgkmcnt(4)
	v_pk_add_f32 v[50:51], v[46:47], v[50:51]
	v_pk_add_f32 v[56:57], v[44:45], v[48:49]
	s_waitcnt lgkmcnt(2)
	v_pk_add_f32 v[46:47], v[40:41], v[36:37]
	v_pk_add_f32 v[48:49], v[38:39], v[34:35]
	ds_read_b128 v[34:37], v116 offset:14336
	v_add_u32_e32 v30, 0x13800, v116
	s_waitcnt lgkmcnt(1)
	v_pk_add_f32 v[40:41], v[108:109], v[112:113]
	ds_read_b128 v[112:115], v30
	v_pk_add_f32 v[44:45], v[106:107], v[110:111]
	ds_read_b128 v[106:109], v116 offset:15360
	v_add_u32_e32 v30, 0x13c00, v116
	ds_read_b128 v[124:127], v30
	s_waitcnt lgkmcnt(2)
	v_pk_add_f32 v[38:39], v[34:35], v[112:113]
	v_pk_mov_b32 v[30:31], v[86:87], v[84:85] op_sel:[1,0]
	v_mov_b32_e32 v34, v86
	v_mov_b32_e32 v35, v85
	v_pk_add_f32 v[136:137], v[30:31], v[34:35]
	v_pk_mov_b32 v[30:31], v[82:83], v[80:81] op_sel:[1,0]
	v_mov_b32_e32 v34, v82
	v_mov_b32_e32 v35, v81
	v_pk_add_f32 v[134:135], v[30:31], v[34:35]
	s_waitcnt lgkmcnt(0)
	v_pk_add_f32 v[30:31], v[108:109], v[126:127]
	v_pk_add_f32 v[34:35], v[106:107], v[124:125]
	v_pk_mov_b32 v[106:107], v[76:77], v[74:75] op_sel:[1,0]
	v_mov_b32_e32 v108, v76
	v_mov_b32_e32 v109, v75
	v_add_f32_e32 v132, v132, v133
	v_pk_add_f32 v[130:131], v[106:107], v[108:109]
	v_pk_mov_b32 v[106:107], v[78:79], v[72:73] op_sel:[1,0]
	v_mov_b32_e32 v108, v78
	v_mov_b32_e32 v109, v73
	v_add_f32_dpp v132, v132, v132 quad_perm:[1,0,3,2] row_mask:0xf bank_mask:0xf bound_ctrl:1
	v_pk_add_f32 v[128:129], v[106:107], v[108:109]
	v_mov_b32_e32 v106, v66
	v_mov_b32_e32 v107, v65
	v_pk_mov_b32 v[108:109], v[66:67], v[64:65] op_sel:[1,0]
	v_add_f32_dpp v132, v132, v132 quad_perm:[2,3,0,1] row_mask:0xf bank_mask:0xf bound_ctrl:1
	v_add_f32_e32 v122, v122, v123
	v_pk_add_f32 v[126:127], v[108:109], v[106:107]
	v_mov_b32_e32 v106, v62
	v_mov_b32_e32 v107, v59
	v_pk_mov_b32 v[108:109], v[62:63], v[58:59] op_sel:[1,0]
	v_add_f32_dpp v132, v132, v132 row_half_mirror row_mask:0xf bank_mask:0xf bound_ctrl:1
	v_add_f32_dpp v122, v122, v122 quad_perm:[1,0,3,2] row_mask:0xf bank_mask:0xf bound_ctrl:1
	v_pk_add_f32 v[124:125], v[108:109], v[106:107]
	v_mov_b32_e32 v106, v54
	v_mov_b32_e32 v107, v53
	v_pk_mov_b32 v[108:109], v[54:55], v[52:53] op_sel:[1,0]
	v_add_f32_dpp v132, v132, v132 row_mirror row_mask:0xf bank_mask:0xf bound_ctrl:1
	v_add_f32_dpp v122, v122, v122 quad_perm:[2,3,0,1] row_mask:0xf bank_mask:0xf bound_ctrl:1
	v_add_f32_e32 v118, v118, v119
	v_pk_add_f32 v[116:117], v[108:109], v[106:107]
	v_mov_b32_e32 v106, v56
	v_mov_b32_e32 v107, v51
	v_pk_mov_b32 v[108:109], v[56:57], v[50:51] op_sel:[1,0]
	v_readlane_b32 s2, v132, 16
	v_readlane_b32 s3, v132, 48
	v_add_f32_dpp v122, v122, v122 row_half_mirror row_mask:0xf bank_mask:0xf bound_ctrl:1
	v_add_f32_dpp v118, v118, v118 quad_perm:[1,0,3,2] row_mask:0xf bank_mask:0xf bound_ctrl:1
	v_pk_add_f32 v[36:37], v[36:37], v[114:115]
	v_pk_add_f32 v[114:115], v[108:109], v[106:107]
	v_mov_b32_e32 v106, v48
	v_mov_b32_e32 v107, v47
	v_pk_mov_b32 v[108:109], v[48:49], v[46:47] op_sel:[1,0]
	v_readlane_b32 s0, v132, 0
	v_readlane_b32 s1, v132, 32
	v_mov_b32_e32 v132, s2
	v_mov_b32_e32 v133, s3
	v_add_f32_dpp v122, v122, v122 row_mirror row_mask:0xf bank_mask:0xf bound_ctrl:1
	v_add_f32_dpp v118, v118, v118 quad_perm:[2,3,0,1] row_mask:0xf bank_mask:0xf bound_ctrl:1
	v_add_f32_e32 v120, v120, v121
	v_pk_add_f32 v[112:113], v[108:109], v[106:107]
	v_mov_b32_e32 v106, v44
	v_mov_b32_e32 v107, v41
	v_pk_mov_b32 v[108:109], v[44:45], v[40:41] op_sel:[1,0]
	v_pk_add_f32 v[132:133], s[0:1], v[132:133]
	v_readlane_b32 s2, v122, 16
	v_readlane_b32 s3, v122, 48
	v_add_f32_dpp v118, v118, v118 row_half_mirror row_mask:0xf bank_mask:0xf bound_ctrl:1
	v_add_f32_dpp v120, v120, v120 quad_perm:[1,0,3,2] row_mask:0xf bank_mask:0xf bound_ctrl:1
	v_pk_add_f32 v[110:111], v[108:109], v[106:107]
	v_mov_b32_e32 v106, v38
	v_mov_b32_e32 v107, v37
	v_pk_mov_b32 v[108:109], v[38:39], v[36:37] op_sel:[1,0]
	v_add_f32_e32 v132, v132, v133
	v_readlane_b32 s0, v122, 0
	v_readlane_b32 s1, v122, 32
	v_mov_b32_e32 v122, s2
	v_mov_b32_e32 v123, s3
	v_add_f32_dpp v118, v118, v118 row_mirror row_mask:0xf bank_mask:0xf bound_ctrl:1
	v_add_f32_dpp v120, v120, v120 quad_perm:[2,3,0,1] row_mask:0xf bank_mask:0xf bound_ctrl:1
	v_add_f32_e32 v136, v136, v137
	v_pk_add_f32 v[108:109], v[108:109], v[106:107]
	v_mov_b32_e32 v106, v34
	v_mov_b32_e32 v107, v31
	v_pk_mov_b32 v[138:139], v[34:35], v[30:31] op_sel:[1,0]
	v_fmamk_f32 v105, v132, 0xbb800000, v105
	v_fmac_f32_e32 v104, 0xbb800000, v132
	v_fmamk_f32 v103, v132, 0xbb800000, v103
	v_fmac_f32_e32 v102, 0xbb800000, v132
	v_pk_add_f32 v[122:123], s[0:1], v[122:123]
	v_readlane_b32 s2, v118, 16
	v_readlane_b32 s3, v118, 48
	v_add_f32_dpp v120, v120, v120 row_half_mirror row_mask:0xf bank_mask:0xf bound_ctrl:1
	v_add_f32_dpp v136, v136, v136 quad_perm:[1,0,3,2] row_mask:0xf bank_mask:0xf bound_ctrl:1
	v_pk_add_f32 v[106:107], v[138:139], v[106:107]
	v_pk_mul_f32 v[132:133], v[102:103], v[102:103]
	v_pk_mul_f32 v[138:139], v[104:105], v[104:105]
	v_add_f32_e32 v122, v122, v123
	v_readlane_b32 s0, v118, 0
	v_readlane_b32 s1, v118, 32
	v_mov_b32_e32 v118, s2
	v_mov_b32_e32 v119, s3
	v_add_f32_dpp v120, v120, v120 row_mirror row_mask:0xf bank_mask:0xf bound_ctrl:1
	v_add_f32_dpp v136, v136, v136 quad_perm:[2,3,0,1] row_mask:0xf bank_mask:0xf bound_ctrl:1
	v_add_f32_e32 v134, v134, v135
	v_pk_mov_b32 v[140:141], v[138:139], v[132:133] op_sel:[1,0]
	v_mov_b32_e32 v139, v133
	v_fmamk_f32 v101, v122, 0xbb800000, v101
	v_fmac_f32_e32 v100, 0xbb800000, v122
	v_fmamk_f32 v99, v122, 0xbb800000, v99
	v_fmac_f32_e32 v98, 0xbb800000, v122
	v_pk_add_f32 v[118:119], s[0:1], v[118:119]
	v_readlane_b32 s2, v120, 16
	v_readlane_b32 s3, v120, 48
	v_add_f32_dpp v136, v136, v136 row_half_mirror row_mask:0xf bank_mask:0xf bound_ctrl:1
	v_add_f32_dpp v134, v134, v134 quad_perm:[1,0,3,2] row_mask:0xf bank_mask:0xf bound_ctrl:1
	v_pk_add_f32 v[132:133], v[140:141], v[138:139]
	v_pk_mul_f32 v[122:123], v[98:99], v[98:99]
	v_pk_mul_f32 v[138:139], v[100:101], v[100:101]
	v_add_f32_e32 v118, v118, v119
	v_readlane_b32 s0, v120, 0
	v_readlane_b32 s1, v120, 32
	v_mov_b32_e32 v120, s2
	v_mov_b32_e32 v121, s3
	v_add_f32_dpp v136, v136, v136 row_mirror row_mask:0xf bank_mask:0xf bound_ctrl:1
	v_add_f32_dpp v134, v134, v134 quad_perm:[2,3,0,1] row_mask:0xf bank_mask:0xf bound_ctrl:1
	v_add_f32_e32 v130, v130, v131
	v_pk_mov_b32 v[140:141], v[138:139], v[122:123] op_sel:[1,0]
	v_mov_b32_e32 v139, v123
	v_fmamk_f32 v95, v118, 0xbb800000, v95
	v_fmac_f32_e32 v94, 0xbb800000, v118
	v_fmamk_f32 v93, v118, 0xbb800000, v93
	v_fmac_f32_e32 v92, 0xbb800000, v118
	v_pk_add_f32 v[120:121], s[0:1], v[120:121]
	v_readlane_b32 s2, v136, 16
	v_readlane_b32 s3, v136, 48
	v_add_f32_dpp v134, v134, v134 row_half_mirror row_mask:0xf bank_mask:0xf bound_ctrl:1
	v_add_f32_dpp v130, v130, v130 quad_perm:[1,0,3,2] row_mask:0xf bank_mask:0xf bound_ctrl:1
	v_pk_add_f32 v[122:123], v[140:141], v[138:139]
	v_pk_mul_f32 v[118:119], v[92:93], v[92:93]
	v_pk_mul_f32 v[138:139], v[94:95], v[94:95]
	v_add_f32_e32 v120, v120, v121
	v_readlane_b32 s0, v136, 0
	v_readlane_b32 s1, v136, 32
	v_mov_b32_e32 v136, s2
	v_mov_b32_e32 v137, s3
	v_add_f32_dpp v134, v134, v134 row_mirror row_mask:0xf bank_mask:0xf bound_ctrl:1
	v_add_f32_dpp v130, v130, v130 quad_perm:[2,3,0,1] row_mask:0xf bank_mask:0xf bound_ctrl:1
	v_add_f32_e32 v128, v128, v129
	v_pk_mov_b32 v[140:141], v[138:139], v[118:119] op_sel:[1,0]
	v_mov_b32_e32 v139, v119
	v_fmamk_f32 v91, v120, 0xbb800000, v91
	v_fmac_f32_e32 v90, 0xbb800000, v120
	v_fmamk_f32 v89, v120, 0xbb800000, v89
	v_fmac_f32_e32 v88, 0xbb800000, v120
	v_pk_add_f32 v[136:137], s[0:1], v[136:137]
	v_readlane_b32 s2, v134, 16
	v_readlane_b32 s3, v134, 48
	v_add_f32_dpp v130, v130, v130 row_half_mirror row_mask:0xf bank_mask:0xf bound_ctrl:1
	v_add_f32_dpp v128, v128, v128 quad_perm:[1,0,3,2] row_mask:0xf bank_mask:0xf bound_ctrl:1
	v_pk_add_f32 v[118:119], v[140:141], v[138:139]
	v_pk_mul_f32 v[120:121], v[88:89], v[88:89]
	v_pk_mul_f32 v[138:139], v[90:91], v[90:91]
	v_add_f32_e32 v136, v136, v137
	v_readlane_b32 s0, v134, 0
	v_readlane_b32 s1, v134, 32
	v_mov_b32_e32 v134, s2
	v_mov_b32_e32 v135, s3
	v_add_f32_dpp v130, v130, v130 row_mirror row_mask:0xf bank_mask:0xf bound_ctrl:1
	v_add_f32_dpp v128, v128, v128 quad_perm:[2,3,0,1] row_mask:0xf bank_mask:0xf bound_ctrl:1
	v_add_f32_e32 v126, v126, v127
	v_pk_mov_b32 v[140:141], v[138:139], v[120:121] op_sel:[1,0]
	v_mov_b32_e32 v139, v121
	v_fmamk_f32 v87, v136, 0xbb800000, v87
	v_fmac_f32_e32 v86, 0xbb800000, v136
	v_fmamk_f32 v85, v136, 0xbb800000, v85
	v_fmac_f32_e32 v84, 0xbb800000, v136
	v_pk_add_f32 v[134:135], s[0:1], v[134:135]
	v_readlane_b32 s2, v130, 16
	v_readlane_b32 s3, v130, 48
	v_add_f32_dpp v128, v128, v128 row_half_mirror row_mask:0xf bank_mask:0xf bound_ctrl:1
	v_add_f32_dpp v126, v126, v126 quad_perm:[1,0,3,2] row_mask:0xf bank_mask:0xf bound_ctrl:1
	v_pk_add_f32 v[120:121], v[140:141], v[138:139]
	v_pk_mul_f32 v[136:137], v[84:85], v[84:85]
	v_pk_mul_f32 v[138:139], v[86:87], v[86:87]
	v_add_f32_e32 v134, v134, v135
	v_readlane_b32 s0, v130, 0
	v_readlane_b32 s1, v130, 32
	v_mov_b32_e32 v130, s2
	v_mov_b32_e32 v131, s3
	v_add_f32_dpp v128, v128, v128 row_mirror row_mask:0xf bank_mask:0xf bound_ctrl:1
	v_add_f32_dpp v126, v126, v126 quad_perm:[2,3,0,1] row_mask:0xf bank_mask:0xf bound_ctrl:1
	v_add_f32_e32 v124, v124, v125
	v_pk_mov_b32 v[140:141], v[138:139], v[136:137] op_sel:[1,0]
	v_mov_b32_e32 v139, v137
	v_fmamk_f32 v83, v134, 0xbb800000, v83
	v_fmac_f32_e32 v82, 0xbb800000, v134
	v_fmamk_f32 v81, v134, 0xbb800000, v81
	v_fmac_f32_e32 v80, 0xbb800000, v134
	v_pk_add_f32 v[130:131], s[0:1], v[130:131]
	v_readlane_b32 s2, v128, 16
	v_readlane_b32 s3, v128, 48
	v_add_f32_dpp v126, v126, v126 row_half_mirror row_mask:0xf bank_mask:0xf bound_ctrl:1
	v_add_f32_dpp v124, v124, v124 quad_perm:[1,0,3,2] row_mask:0xf bank_mask:0xf bound_ctrl:1
	v_pk_add_f32 v[136:137], v[140:141], v[138:139]
	v_pk_mul_f32 v[134:135], v[80:81], v[80:81]
	v_pk_mul_f32 v[138:139], v[82:83], v[82:83]
	v_add_f32_e32 v130, v130, v131
	v_readlane_b32 s0, v128, 0
	v_readlane_b32 s1, v128, 32
	v_mov_b32_e32 v128, s2
	v_mov_b32_e32 v129, s3
	v_add_f32_dpp v126, v126, v126 row_mirror row_mask:0xf bank_mask:0xf bound_ctrl:1
	v_add_f32_dpp v124, v124, v124 quad_perm:[2,3,0,1] row_mask:0xf bank_mask:0xf bound_ctrl:1
	v_add_f32_e32 v116, v116, v117
	v_pk_mov_b32 v[140:141], v[138:139], v[134:135] op_sel:[1,0]
	v_mov_b32_e32 v139, v135
	v_fmamk_f32 v77, v130, 0xbb800000, v77
	v_fmac_f32_e32 v76, 0xbb800000, v130
	v_fmamk_f32 v75, v130, 0xbb800000, v75
	v_fmac_f32_e32 v74, 0xbb800000, v130
	v_pk_add_f32 v[128:129], s[0:1], v[128:129]
	v_readlane_b32 s2, v126, 16
	v_readlane_b32 s3, v126, 48
	v_add_f32_dpp v124, v124, v124 row_half_mirror row_mask:0xf bank_mask:0xf bound_ctrl:1
	v_add_f32_dpp v116, v116, v116 quad_perm:[1,0,3,2] row_mask:0xf bank_mask:0xf bound_ctrl:1
	v_pk_add_f32 v[134:135], v[140:141], v[138:139]
	v_pk_mul_f32 v[130:131], v[74:75], v[74:75]
	v_pk_mul_f32 v[138:139], v[76:77], v[76:77]
	v_add_f32_e32 v128, v128, v129
	v_readlane_b32 s0, v126, 0
	v_readlane_b32 s1, v126, 32
	v_mov_b32_e32 v126, s2
	v_mov_b32_e32 v127, s3
	v_add_f32_dpp v124, v124, v124 row_mirror row_mask:0xf bank_mask:0xf bound_ctrl:1
	v_add_f32_dpp v116, v116, v116 quad_perm:[2,3,0,1] row_mask:0xf bank_mask:0xf bound_ctrl:1
	v_add_f32_e32 v114, v114, v115
	v_pk_mov_b32 v[140:141], v[138:139], v[130:131] op_sel:[1,0]
	v_mov_b32_e32 v139, v131
	v_fmamk_f32 v79, v128, 0xbb800000, v79
	v_fmac_f32_e32 v78, 0xbb800000, v128
	v_fmamk_f32 v73, v128, 0xbb800000, v73
	v_fmac_f32_e32 v72, 0xbb800000, v128
	v_pk_add_f32 v[126:127], s[0:1], v[126:127]
	v_readlane_b32 s2, v124, 16
	v_readlane_b32 s3, v124, 48
	v_add_f32_dpp v116, v116, v116 row_half_mirror row_mask:0xf bank_mask:0xf bound_ctrl:1
	v_add_f32_dpp v114, v114, v114 quad_perm:[1,0,3,2] row_mask:0xf bank_mask:0xf bound_ctrl:1
	v_pk_add_f32 v[130:131], v[140:141], v[138:139]
	v_pk_mul_f32 v[128:129], v[72:73], v[72:73]
	v_pk_mul_f32 v[138:139], v[78:79], v[78:79]
	v_add_f32_e32 v126, v126, v127
	v_readlane_b32 s0, v124, 0
	v_readlane_b32 s1, v124, 32
	v_mov_b32_e32 v124, s2
	v_mov_b32_e32 v125, s3
	v_add_f32_dpp v116, v116, v116 row_mirror row_mask:0xf bank_mask:0xf bound_ctrl:1
	v_add_f32_dpp v114, v114, v114 quad_perm:[2,3,0,1] row_mask:0xf bank_mask:0xf bound_ctrl:1
	v_add_f32_e32 v112, v112, v113
	v_pk_mov_b32 v[140:141], v[138:139], v[128:129] op_sel:[1,0]
	v_mov_b32_e32 v139, v129
	v_fmamk_f32 v67, v126, 0xbb800000, v67
	v_fmac_f32_e32 v66, 0xbb800000, v126
	v_fmamk_f32 v65, v126, 0xbb800000, v65
	v_fmac_f32_e32 v64, 0xbb800000, v126
	v_pk_add_f32 v[124:125], s[0:1], v[124:125]
	v_readlane_b32 s2, v116, 16
	v_readlane_b32 s3, v116, 48
	v_add_f32_dpp v114, v114, v114 row_half_mirror row_mask:0xf bank_mask:0xf bound_ctrl:1
	v_add_f32_dpp v112, v112, v112 quad_perm:[1,0,3,2] row_mask:0xf bank_mask:0xf bound_ctrl:1
	v_pk_add_f32 v[128:129], v[140:141], v[138:139]
	v_pk_mul_f32 v[126:127], v[64:65], v[64:65]
	v_pk_mul_f32 v[138:139], v[66:67], v[66:67]
	v_add_f32_e32 v124, v124, v125
	v_readlane_b32 s0, v116, 0
	v_readlane_b32 s1, v116, 32
	v_mov_b32_e32 v116, s2
	v_mov_b32_e32 v117, s3
	v_add_f32_dpp v114, v114, v114 row_mirror row_mask:0xf bank_mask:0xf bound_ctrl:1
	v_add_f32_dpp v112, v112, v112 quad_perm:[2,3,0,1] row_mask:0xf bank_mask:0xf bound_ctrl:1
	v_add_f32_e32 v110, v110, v111
	v_pk_mov_b32 v[140:141], v[138:139], v[126:127] op_sel:[1,0]
	v_mov_b32_e32 v139, v127
	v_fmamk_f32 v63, v124, 0xbb800000, v63
	v_fmac_f32_e32 v62, 0xbb800000, v124
	v_fmamk_f32 v59, v124, 0xbb800000, v59
	v_fmac_f32_e32 v58, 0xbb800000, v124
	v_pk_add_f32 v[116:117], s[0:1], v[116:117]
	v_readlane_b32 s2, v114, 16
	v_readlane_b32 s3, v114, 48
	v_add_f32_dpp v112, v112, v112 row_half_mirror row_mask:0xf bank_mask:0xf bound_ctrl:1
	v_add_f32_dpp v110, v110, v110 quad_perm:[1,0,3,2] row_mask:0xf bank_mask:0xf bound_ctrl:1
	v_pk_add_f32 v[126:127], v[140:141], v[138:139]
	v_pk_mul_f32 v[124:125], v[58:59], v[58:59]
	v_pk_mul_f32 v[138:139], v[62:63], v[62:63]
	v_add_f32_e32 v116, v116, v117
	v_readlane_b32 s0, v114, 0
	v_readlane_b32 s1, v114, 32
	v_mov_b32_e32 v114, s2
	v_mov_b32_e32 v115, s3
	v_add_f32_dpp v112, v112, v112 row_mirror row_mask:0xf bank_mask:0xf bound_ctrl:1
	v_add_f32_dpp v110, v110, v110 quad_perm:[2,3,0,1] row_mask:0xf bank_mask:0xf bound_ctrl:1
	v_add_f32_e32 v108, v108, v109
	v_pk_mov_b32 v[140:141], v[138:139], v[124:125] op_sel:[1,0]
	v_mov_b32_e32 v139, v125
	v_fmamk_f32 v55, v116, 0xbb800000, v55
	v_fmac_f32_e32 v54, 0xbb800000, v116
	v_fmamk_f32 v53, v116, 0xbb800000, v53
	v_fmac_f32_e32 v52, 0xbb800000, v116
	v_pk_add_f32 v[114:115], s[0:1], v[114:115]
	v_readlane_b32 s2, v112, 16
	v_readlane_b32 s3, v112, 48
	v_add_f32_dpp v110, v110, v110 row_half_mirror row_mask:0xf bank_mask:0xf bound_ctrl:1
	v_add_f32_dpp v108, v108, v108 quad_perm:[1,0,3,2] row_mask:0xf bank_mask:0xf bound_ctrl:1
	v_pk_add_f32 v[124:125], v[140:141], v[138:139]
	v_pk_mul_f32 v[116:117], v[52:53], v[52:53]
	v_pk_mul_f32 v[138:139], v[54:55], v[54:55]
	v_add_f32_e32 v114, v114, v115
	v_readlane_b32 s0, v112, 0
	v_readlane_b32 s1, v112, 32
	v_mov_b32_e32 v112, s2
	v_mov_b32_e32 v113, s3
	v_add_f32_dpp v110, v110, v110 row_mirror row_mask:0xf bank_mask:0xf bound_ctrl:1
	v_add_f32_dpp v108, v108, v108 quad_perm:[2,3,0,1] row_mask:0xf bank_mask:0xf bound_ctrl:1
	v_add_f32_e32 v106, v106, v107
	v_pk_mov_b32 v[140:141], v[138:139], v[116:117] op_sel:[1,0]
	v_mov_b32_e32 v139, v117
	v_fmamk_f32 v57, v114, 0xbb800000, v57
	v_fmac_f32_e32 v56, 0xbb800000, v114
	v_fmamk_f32 v51, v114, 0xbb800000, v51
	v_fmac_f32_e32 v50, 0xbb800000, v114
	v_pk_add_f32 v[112:113], s[0:1], v[112:113]
	v_readlane_b32 s2, v110, 16
	v_readlane_b32 s3, v110, 48
	v_add_f32_dpp v108, v108, v108 row_half_mirror row_mask:0xf bank_mask:0xf bound_ctrl:1
	v_add_f32_dpp v106, v106, v106 quad_perm:[1,0,3,2] row_mask:0xf bank_mask:0xf bound_ctrl:1
	v_pk_add_f32 v[116:117], v[140:141], v[138:139]
	v_pk_mul_f32 v[114:115], v[50:51], v[50:51]
	v_pk_mul_f32 v[138:139], v[56:57], v[56:57]
	v_add_f32_e32 v112, v112, v113
	v_readlane_b32 s0, v110, 0
	v_readlane_b32 s1, v110, 32
	v_mov_b32_e32 v110, s2
	v_mov_b32_e32 v111, s3
	v_add_f32_dpp v108, v108, v108 row_mirror row_mask:0xf bank_mask:0xf bound_ctrl:1
	v_add_f32_dpp v106, v106, v106 quad_perm:[2,3,0,1] row_mask:0xf bank_mask:0xf bound_ctrl:1
	v_pk_mov_b32 v[140:141], v[138:139], v[114:115] op_sel:[1,0]
	v_mov_b32_e32 v139, v115
	v_fmamk_f32 v49, v112, 0xbb800000, v49
	v_fmac_f32_e32 v48, 0xbb800000, v112
	v_fmamk_f32 v47, v112, 0xbb800000, v47
	v_fmac_f32_e32 v46, 0xbb800000, v112
	v_pk_add_f32 v[110:111], s[0:1], v[110:111]
	v_readlane_b32 s2, v108, 16
	v_readlane_b32 s3, v108, 48
	v_add_f32_dpp v106, v106, v106 row_half_mirror row_mask:0xf bank_mask:0xf bound_ctrl:1
	v_pk_add_f32 v[114:115], v[140:141], v[138:139]
	v_pk_mul_f32 v[112:113], v[46:47], v[46:47]
	v_pk_mul_f32 v[138:139], v[48:49], v[48:49]
	v_add_f32_e32 v110, v110, v111
	v_readlane_b32 s0, v108, 0
	v_readlane_b32 s1, v108, 32
	v_mov_b32_e32 v108, s2
	v_mov_b32_e32 v109, s3
	v_add_f32_dpp v106, v106, v106 row_mirror row_mask:0xf bank_mask:0xf bound_ctrl:1
	v_pk_mov_b32 v[140:141], v[138:139], v[112:113] op_sel:[1,0]
	v_mov_b32_e32 v139, v113
	v_fmamk_f32 v45, v110, 0xbb800000, v45
	v_fmac_f32_e32 v44, 0xbb800000, v110
	v_fmamk_f32 v41, v110, 0xbb800000, v41
	v_fmac_f32_e32 v40, 0xbb800000, v110
	v_pk_add_f32 v[108:109], s[0:1], v[108:109]
	v_readlane_b32 s2, v106, 16
	v_readlane_b32 s3, v106, 48
	v_pk_add_f32 v[112:113], v[140:141], v[138:139]
	v_pk_mul_f32 v[110:111], v[40:41], v[40:41]
	v_pk_mul_f32 v[138:139], v[44:45], v[44:45]
	v_add_f32_e32 v108, v108, v109
	v_readlane_b32 s0, v106, 0
	v_readlane_b32 s1, v106, 32
	v_mov_b32_e32 v106, s2
	v_mov_b32_e32 v107, s3
	v_pk_mov_b32 v[140:141], v[138:139], v[110:111] op_sel:[1,0]
	v_mov_b32_e32 v139, v111
	v_fmamk_f32 v39, v108, 0xbb800000, v39
	v_fmac_f32_e32 v38, 0xbb800000, v108
	v_fmamk_f32 v37, v108, 0xbb800000, v37
	v_fmac_f32_e32 v36, 0xbb800000, v108
	v_pk_add_f32 v[106:107], s[0:1], v[106:107]
	v_pk_add_f32 v[110:111], v[140:141], v[138:139]
	v_pk_mul_f32 v[108:109], v[36:37], v[36:37]
	v_pk_mul_f32 v[138:139], v[38:39], v[38:39]
	v_add_f32_e32 v106, v106, v107
	v_pk_mov_b32 v[140:141], v[138:139], v[108:109] op_sel:[1,0]
	v_mov_b32_e32 v139, v109
	v_fmamk_f32 v35, v106, 0xbb800000, v35
	v_fmac_f32_e32 v34, 0xbb800000, v106
	v_fmamk_f32 v31, v106, 0xbb800000, v31
	v_fmac_f32_e32 v30, 0xbb800000, v106
	v_pk_add_f32 v[108:109], v[140:141], v[138:139]
	v_pk_mul_f32 v[106:107], v[30:31], v[30:31]
	v_pk_mul_f32 v[138:139], v[34:35], v[34:35]
	v_add_f32_e32 v132, v132, v133
	v_pk_mov_b32 v[140:141], v[138:139], v[106:107] op_sel:[1,0]
	v_mov_b32_e32 v139, v107
	v_pk_add_f32 v[106:107], v[140:141], v[138:139]
	v_add_f32_e32 v122, v122, v123
	v_add_f32_e32 v133, v106, v107
	v_add_f32_dpp v106, v132, v132 quad_perm:[1,0,3,2] row_mask:0xf bank_mask:0xf bound_ctrl:1
	v_add_f32_e32 v123, v130, v131
	v_add_f32_e32 v131, v108, v109
	v_add_f32_dpp v106, v106, v106 quad_perm:[2,3,0,1] row_mask:0xf bank_mask:0xf bound_ctrl:1
	v_add_f32_e32 v118, v118, v119
	v_add_f32_e32 v130, v110, v111
	v_add_f32_dpp v106, v106, v106 row_half_mirror row_mask:0xf bank_mask:0xf bound_ctrl:1
	v_add_f32_e32 v119, v120, v121
	v_add_f32_e32 v120, v136, v137
	v_add_f32_dpp v106, v106, v106 row_mirror row_mask:0xf bank_mask:0xf bound_ctrl:1
	v_add_f32_e32 v128, v128, v129
	v_readlane_b32 s2, v106, 16
	v_readlane_b32 s3, v106, 48
	v_readlane_b32 s0, v106, 0
	v_readlane_b32 s1, v106, 32
	v_mov_b32_e32 v106, s2
	v_mov_b32_e32 v107, s3
	v_pk_add_f32 v[108:109], s[0:1], v[106:107]
	v_add_f32_dpp v106, v122, v122 quad_perm:[1,0,3,2] row_mask:0xf bank_mask:0xf bound_ctrl:1
	v_add_f32_e32 v129, v112, v113
	v_add_f32_dpp v112, v120, v120 quad_perm:[1,0,3,2] row_mask:0xf bank_mask:0xf bound_ctrl:1
	v_add_f32_dpp v106, v106, v106 quad_perm:[2,3,0,1] row_mask:0xf bank_mask:0xf bound_ctrl:1
	v_add_f32_e32 v121, v134, v135
	v_add_f32_dpp v112, v112, v112 quad_perm:[2,3,0,1] row_mask:0xf bank_mask:0xf bound_ctrl:1
	v_add_f32_dpp v106, v106, v106 row_half_mirror row_mask:0xf bank_mask:0xf bound_ctrl:1
	v_add_f32_e32 v126, v126, v127
	v_add_f32_dpp v112, v112, v112 row_half_mirror row_mask:0xf bank_mask:0xf bound_ctrl:1
	v_add_f32_dpp v106, v106, v106 row_mirror row_mask:0xf bank_mask:0xf bound_ctrl:1
	v_add_f32_e32 v127, v114, v115
	v_readlane_b32 s2, v106, 16
	v_readlane_b32 s3, v106, 48
	v_readlane_b32 s0, v106, 0
	v_readlane_b32 s1, v106, 32
	v_mov_b32_e32 v106, s2
	v_mov_b32_e32 v107, s3
	v_pk_add_f32 v[110:111], s[0:1], v[106:107]
	v_add_f32_dpp v106, v118, v118 quad_perm:[1,0,3,2] row_mask:0xf bank_mask:0xf bound_ctrl:1
	v_add_f32_dpp v112, v112, v112 row_mirror row_mask:0xf bank_mask:0xf bound_ctrl:1
	v_add_f32_dpp v114, v123, v123 quad_perm:[1,0,3,2] row_mask:0xf bank_mask:0xf bound_ctrl:1
	v_add_f32_dpp v106, v106, v106 quad_perm:[2,3,0,1] row_mask:0xf bank_mask:0xf bound_ctrl:1
	v_readlane_b32 s23, v112, 16
	v_readlane_b32 s24, v112, 48
	v_add_f32_dpp v106, v106, v106 row_half_mirror row_mask:0xf bank_mask:0xf bound_ctrl:1
	v_add_f32_dpp v114, v114, v114 quad_perm:[2,3,0,1] row_mask:0xf bank_mask:0xf bound_ctrl:1
	v_add_f32_e32 v124, v124, v125
	v_add_f32_dpp v106, v106, v106 row_mirror row_mask:0xf bank_mask:0xf bound_ctrl:1
	v_add_f32_dpp v114, v114, v114 row_half_mirror row_mask:0xf bank_mask:0xf bound_ctrl:1
	v_readlane_b32 s0, v106, 0
	v_readlane_b32 s2, v106, 16
	v_readlane_b32 s1, v106, 32
	v_readlane_b32 s3, v106, 48
	v_add_f32_dpp v106, v119, v119 quad_perm:[1,0,3,2] row_mask:0xf bank_mask:0xf bound_ctrl:1
	v_add_f32_dpp v114, v114, v114 row_mirror row_mask:0xf bank_mask:0xf bound_ctrl:1
	v_mov_b32_e32 v107, s3
	v_add_f32_dpp v106, v106, v106 quad_perm:[2,3,0,1] row_mask:0xf bank_mask:0xf bound_ctrl:1
	v_readlane_b32 s21, v114, 16
	v_readlane_b32 s22, v114, 48
	v_add_f32_dpp v106, v106, v106 row_half_mirror row_mask:0xf bank_mask:0xf bound_ctrl:1
	v_add_f32_e32 v125, v116, v117
	v_cvt_f32_f16_sdwa v115, v96 dst_sel:DWORD dst_unused:UNUSED_PAD src0_sel:WORD_1
	v_add_f32_dpp v106, v106, v106 row_mirror row_mask:0xf bank_mask:0xf bound_ctrl:1
	v_cvt_f32_f16_e32 v116, v97
	v_readlane_b32 s4, v106, 0
	v_readlane_b32 s6, v106, 16
	v_readlane_b32 s5, v106, 32
	v_readlane_b32 s7, v106, 48
	v_mov_b32_e32 v106, s2
	v_pk_add_f32 v[106:107], s[0:1], v[106:107]
	v_readlane_b32 s0, v112, 0
	v_readlane_b32 s1, v112, 32
	v_add_f32_dpp v112, v121, v121 quad_perm:[1,0,3,2] row_mask:0xf bank_mask:0xf bound_ctrl:1
	v_mov_b32_e32 v113, s7
	v_cvt_f32_f16_sdwa v117, v97 dst_sel:DWORD dst_unused:UNUSED_PAD src0_sel:WORD_1
	v_add_f32_dpp v112, v112, v112 quad_perm:[2,3,0,1] row_mask:0xf bank_mask:0xf bound_ctrl:1
	v_mov_b32_e32 v97, v108
	v_mov_b32_e32 v108, v111
	v_add_f32_dpp v112, v112, v112 row_half_mirror row_mask:0xf bank_mask:0xf bound_ctrl:1
	v_mov_b32_e32 v111, s24
	s_nop 0
	v_add_f32_dpp v112, v112, v112 row_mirror row_mask:0xf bank_mask:0xf bound_ctrl:1
	s_nop 0
	v_readlane_b32 s2, v112, 0
	v_readlane_b32 s19, v112, 16
	v_readlane_b32 s3, v112, 32
	v_readlane_b32 s20, v112, 48
	v_mov_b32_e32 v112, s6
	v_pk_add_f32 v[112:113], s[4:5], v[112:113]
	v_readlane_b32 s4, v114, 0
	v_readlane_b32 s5, v114, 32
	v_add_f32_dpp v114, v128, v128 quad_perm:[1,0,3,2] row_mask:0xf bank_mask:0xf bound_ctrl:1
	s_nop 1
	v_add_f32_dpp v114, v114, v114 quad_perm:[2,3,0,1] row_mask:0xf bank_mask:0xf bound_ctrl:1
	s_nop 1
	v_add_f32_dpp v114, v114, v114 row_half_mirror row_mask:0xf bank_mask:0xf bound_ctrl:1
	s_nop 1
	v_add_f32_dpp v114, v114, v114 row_mirror row_mask:0xf bank_mask:0xf bound_ctrl:1
	s_nop 0
	v_readlane_b32 s6, v114, 0
	v_readlane_b32 s29, v114, 16
	v_readlane_b32 s7, v114, 32
	v_readlane_b32 s30, v114, 48
	v_add_f32_dpp v114, v126, v126 quad_perm:[1,0,3,2] row_mask:0xf bank_mask:0xf bound_ctrl:1
	s_nop 1
	v_add_f32_dpp v114, v114, v114 quad_perm:[2,3,0,1] row_mask:0xf bank_mask:0xf bound_ctrl:1
	s_nop 1
	v_add_f32_dpp v114, v114, v114 row_half_mirror row_mask:0xf bank_mask:0xf bound_ctrl:1
	s_nop 1
	v_add_f32_dpp v114, v114, v114 row_mirror row_mask:0xf bank_mask:0xf bound_ctrl:1
	s_nop 0
	v_readlane_b32 s10, v114, 0
	v_readlane_b32 s31, v114, 16
	v_readlane_b32 s11, v114, 32
	v_readlane_b32 s33, v114, 48
	v_add_f32_dpp v114, v124, v124 quad_perm:[1,0,3,2] row_mask:0xf bank_mask:0xf bound_ctrl:1
	v_cvt_f32_f16_e32 v124, v69
	s_nop 0
	v_add_f32_dpp v114, v114, v114 quad_perm:[2,3,0,1] row_mask:0xf bank_mask:0xf bound_ctrl:1
	s_nop 1
	v_add_f32_dpp v114, v114, v114 row_half_mirror row_mask:0xf bank_mask:0xf bound_ctrl:1
	s_nop 1
	v_add_f32_dpp v114, v114, v114 row_mirror row_mask:0xf bank_mask:0xf bound_ctrl:1
	s_nop 0
	v_readlane_b32 s8, v114, 0
	v_readlane_b32 s34, v114, 16
	v_readlane_b32 s9, v114, 32
	v_readlane_b32 s35, v114, 48
	v_cvt_f32_f16_e32 v114, v96
	v_mov_b32_e32 v96, v110
	v_mov_b32_e32 v110, s23
	v_pk_add_f32 v[118:119], s[0:1], v[110:111]
	v_pk_add_f32 v[108:109], v[96:97], v[108:109]
	v_add_f32_dpp v110, v125, v125 quad_perm:[1,0,3,2] row_mask:0xf bank_mask:0xf bound_ctrl:1
	s_mov_b32 s0, 0x3b800000
	v_mov_b64_e32 v[96:97], s[28:29]
	v_add_f32_dpp v110, v110, v110 quad_perm:[2,3,0,1] row_mask:0xf bank_mask:0xf bound_ctrl:1
	v_cvt_f32_f16_sdwa v125, v69 dst_sel:DWORD dst_unused:UNUSED_PAD src0_sel:WORD_1
	v_mov_b32_e32 v69, v106
	v_add_f32_dpp v110, v110, v110 row_half_mirror row_mask:0xf bank_mask:0xf bound_ctrl:1
	v_mov_b32_e32 v106, v113
	s_nop 0
	v_add_f32_dpp v110, v110, v110 row_mirror row_mask:0xf bank_mask:0xf bound_ctrl:1
	s_nop 0
	v_readlane_b32 s24, v110, 0
	v_readlane_b32 s23, v110, 16
	v_readlane_b32 s25, v110, 32
	v_readlane_b32 s36, v110, 48
	v_add_f32_dpp v110, v127, v127 quad_perm:[1,0,3,2] row_mask:0xf bank_mask:0xf bound_ctrl:1
	s_nop 1
	v_add_f32_dpp v110, v110, v110 quad_perm:[2,3,0,1] row_mask:0xf bank_mask:0xf bound_ctrl:1
	s_nop 1
	v_add_f32_dpp v110, v110, v110 row_half_mirror row_mask:0xf bank_mask:0xf bound_ctrl:1
	s_nop 1
	v_add_f32_dpp v120, v110, v110 row_mirror row_mask:0xf bank_mask:0xf bound_ctrl:1
	v_pk_fma_f32 v[110:111], v[108:109], s[0:1], v[96:97] op_sel_hi:[1,0,0]
	s_mov_b32 s1, 0x800000
	v_mul_f32_e32 v108, 0x4b800000, v111
	v_cmp_gt_f32_e32 vcc, s1, v111
	v_readlane_b32 s26, v120, 0
	v_readlane_b32 s28, v120, 16
	v_cndmask_b32_e32 v108, v111, v108, vcc
	v_rsq_f32_e32 v108, v108
	v_readlane_b32 s27, v120, 32
	v_readlane_b32 s37, v120, 48
	v_mul_f32_e32 v109, 0x45800000, v108
	v_cndmask_b32_e32 v108, v108, v109, vcc
	v_pk_mul_f32 v[104:105], v[108:109], v[104:105] op_sel_hi:[0,1]
	v_pk_mul_f32 v[102:103], v[108:109], v[102:103] op_sel_hi:[0,1]
	v_pk_fma_f32 v[104:105], v[0:1], v[104:105], v[4:5]
	v_pk_fma_f32 v[102:103], v[2:3], v[102:103], v[6:7]
	v_pk_mul_f32 v[104:105], v[104:105], v[114:115]
	v_mov_b32_e32 v114, s19
	v_mov_b32_e32 v115, s20
	v_mov_b32_e32 v108, s21
	v_mov_b32_e32 v109, s22
	v_pk_mul_f32 v[102:103], v[102:103], v[116:117]
	v_pk_add_f32 v[120:121], s[2:3], v[114:115]
	v_pk_add_f32 v[114:115], s[4:5], v[108:109]
	v_mov_b32_e32 v108, s29
	v_mov_b32_e32 v109, s30
	v_cvt_pk_f16_f32 v104, v104, v105
	v_cvt_pk_f16_f32 v105, v102, v103
	v_mov_b32_e32 v102, s31
	v_mov_b32_e32 v103, s33
	v_pk_add_f32 v[116:117], s[6:7], v[108:109]
	v_pk_add_f32 v[108:109], s[10:11], v[102:103]
	v_add_f32_dpp v102, v129, v129 quad_perm:[1,0,3,2] row_mask:0xf bank_mask:0xf bound_ctrl:1
	v_cmp_gt_f32_e32 vcc, s1, v110
	v_mov_b32_e32 v103, s35
	v_add_f32_dpp v102, v102, v102 quad_perm:[2,3,0,1] row_mask:0xf bank_mask:0xf bound_ctrl:1
	global_store_dwordx2 v[60:61], v[104:105], off sc1
	v_mov_b32_e32 v105, s37
	v_add_f32_dpp v102, v102, v102 row_half_mirror row_mask:0xf bank_mask:0xf bound_ctrl:1
	s_nop 1
	v_add_f32_dpp v102, v102, v102 row_mirror row_mask:0xf bank_mask:0xf bound_ctrl:1
	s_nop 0
	v_readlane_b32 s2, v102, 0
	v_readlane_b32 s6, v102, 16
	v_readlane_b32 s3, v102, 32
	v_readlane_b32 s7, v102, 48
	v_mul_f32_e32 v102, 0x4b800000, v110
	v_cndmask_b32_e32 v122, v110, v102, vcc
	v_mov_b32_e32 v102, s34
	v_rsq_f32_e32 v122, v122
	v_pk_add_f32 v[110:111], s[8:9], v[102:103]
	v_add_f32_dpp v102, v130, v130 quad_perm:[1,0,3,2] row_mask:0xf bank_mask:0xf bound_ctrl:1
	v_cvt_f32_f16_sdwa v103, v70 dst_sel:DWORD dst_unused:UNUSED_PAD src0_sel:WORD_1
	v_mul_f32_e32 v104, 0x45800000, v122
	v_add_f32_dpp v102, v102, v102 quad_perm:[2,3,0,1] row_mask:0xf bank_mask:0xf bound_ctrl:1
	s_nop 1
	v_add_f32_dpp v102, v102, v102 row_half_mirror row_mask:0xf bank_mask:0xf bound_ctrl:1
	s_nop 1
	v_add_f32_dpp v102, v102, v102 row_mirror row_mask:0xf bank_mask:0xf bound_ctrl:1
	s_nop 0
	v_readlane_b32 s4, v102, 0
	v_readlane_b32 s8, v102, 16
	v_readlane_b32 s5, v102, 32
	v_readlane_b32 s9, v102, 48
	v_cvt_f32_f16_e32 v102, v70
	v_cndmask_b32_e32 v70, v122, v104, vcc
	v_pk_mul_f32 v[100:101], v[70:71], v[100:101] op_sel_hi:[0,1]
	v_pk_mul_f32 v[98:99], v[70:71], v[98:99] op_sel_hi:[0,1]
	v_cvt_f32_f16_e32 v70, v71
	v_cvt_f32_f16_sdwa v71, v71 dst_sel:DWORD dst_unused:UNUSED_PAD src0_sel:WORD_1
	v_pk_fma_f32 v[100:101], v[0:1], v[100:101], v[4:5]
	v_pk_fma_f32 v[98:99], v[2:3], v[98:99], v[6:7]
	v_pk_mul_f32 v[100:101], v[100:101], v[102:103]
	v_pk_mul_f32 v[70:71], v[98:99], v[70:71]
	v_cvt_pk_f16_f32 v100, v100, v101
	v_cvt_pk_f16_f32 v101, v70, v71
	v_cvt_f32_f16_e32 v70, v68
	v_cvt_f32_f16_sdwa v71, v68 dst_sel:DWORD dst_unused:UNUSED_PAD src0_sel:WORD_1
	v_mov_b32_e32 v68, v112
	v_pk_add_f32 v[68:69], v[68:69], v[106:107]
	v_add_f32_dpp v106, v131, v131 quad_perm:[1,0,3,2] row_mask:0xf bank_mask:0xf bound_ctrl:1
	v_mov_b32_e32 v98, s6
	v_mov_b32_e32 v99, s7
	v_add_f32_dpp v106, v106, v106 quad_perm:[2,3,0,1] row_mask:0xf bank_mask:0xf bound_ctrl:1
	v_pk_add_f32 v[98:99], s[2:3], v[98:99]
	v_add_co_u32_e32 v122, vcc, s18, v60
	v_add_f32_dpp v106, v106, v106 row_half_mirror row_mask:0xf bank_mask:0xf bound_ctrl:1
	s_nop 0
	v_addc_co_u32_e32 v123, vcc, 0, v61, vcc
	v_add_f32_dpp v106, v106, v106 row_mirror row_mask:0xf bank_mask:0xf bound_ctrl:1
	global_store_dwordx2 v[122:123], v[100:101], off offset:-4096 sc1
	v_readlane_b32 s2, v106, 0
	v_readlane_b32 s6, v106, 16
	v_readlane_b32 s3, v106, 32
	v_readlane_b32 s7, v106, 48
	v_add_f32_dpp v106, v133, v133 quad_perm:[1,0,3,2] row_mask:0xf bank_mask:0xf bound_ctrl:1
	v_mov_b32_e32 v100, s8
	v_mov_b32_e32 v101, s9
	v_add_f32_dpp v106, v106, v106 quad_perm:[2,3,0,1] row_mask:0xf bank_mask:0xf bound_ctrl:1
	v_pk_add_f32 v[100:101], s[4:5], v[100:101]
	v_mov_b32_e32 v102, s23
	v_add_f32_dpp v106, v106, v106 row_half_mirror row_mask:0xf bank_mask:0xf bound_ctrl:1
	v_mov_b32_e32 v103, s36
	v_mov_b32_e32 v104, s28
	v_add_f32_dpp v112, v106, v106 row_mirror row_mask:0xf bank_mask:0xf bound_ctrl:1
	v_pk_fma_f32 v[106:107], v[68:69], s[0:1], v[96:97] op_sel_hi:[1,0,0]
	v_readlane_b32 s4, v112, 0
	v_mul_f32_e32 v68, 0x4b800000, v107
	v_cmp_gt_f32_e32 vcc, s1, v107
	v_readlane_b32 s8, v112, 16
	v_readlane_b32 s5, v112, 32
	v_cndmask_b32_e32 v68, v107, v68, vcc
	v_rsq_f32_e32 v68, v68
	v_readlane_b32 s9, v112, 48
	v_pk_add_f32 v[102:103], s[24:25], v[102:103]
	v_pk_add_f32 v[104:105], s[26:27], v[104:105]
	v_mul_f32_e32 v69, 0x45800000, v68
	v_cndmask_b32_e32 v112, v68, v69, vcc
	v_pk_mul_f32 v[68:69], v[112:113], v[94:95] op_sel_hi:[0,1]
	v_pk_fma_f32 v[68:69], v[0:1], v[68:69], v[4:5]
	v_cmp_gt_f32_e32 vcc, s1, v106
	v_pk_mul_f32 v[94:95], v[68:69], v[70:71]
	v_mul_f32_e32 v70, 0x4b800000, v106
	v_cndmask_b32_e32 v106, v106, v70, vcc
	v_pk_mul_f32 v[92:93], v[112:113], v[92:93] op_sel_hi:[0,1]
	v_rsq_f32_e32 v106, v106
	v_pk_fma_f32 v[92:93], v[2:3], v[92:93], v[6:7]
	v_cvt_pk_f16_f32 v94, v94, v95
	v_pk_mul_f32 v[92:93], v[92:93], v[124:125]
	v_mov_b32_e32 v68, s6
	v_cvt_pk_f16_f32 v95, v92, v93
	global_store_dwordx2 v[122:123], v[94:95], off sc1
	v_mul_f32_e32 v94, 0x45800000, v106
	v_cvt_f32_f16_e32 v92, v42
	v_cvt_f32_f16_sdwa v93, v42 dst_sel:DWORD dst_unused:UNUSED_PAD src0_sel:WORD_1
	v_cndmask_b32_e32 v42, v106, v94, vcc
	v_pk_mul_f32 v[90:91], v[42:43], v[90:91] op_sel_hi:[0,1]
	v_pk_fma_f32 v[90:91], v[0:1], v[90:91], v[4:5]
	v_mov_b32_e32 v69, s7
	v_pk_mul_f32 v[90:91], v[90:91], v[92:93]
	v_cvt_f32_f16_e32 v92, v43
	v_cvt_f32_f16_sdwa v93, v43 dst_sel:DWORD dst_unused:UNUSED_PAD src0_sel:WORD_1
	v_pk_mul_f32 v[42:43], v[42:43], v[88:89] op_sel_hi:[0,1]
	v_pk_fma_f32 v[42:43], v[2:3], v[42:43], v[6:7]
	v_cvt_pk_f16_f32 v90, v90, v91
	v_pk_mul_f32 v[42:43], v[42:43], v[92:93]
	v_cvt_f32_f16_e32 v88, v32
	v_cvt_pk_f16_f32 v91, v42, v43
	v_add_co_u32_e32 v42, vcc, s17, v60
	v_mov_b32_e32 v70, s8
	s_nop 0
	v_addc_co_u32_e32 v43, vcc, 0, v61, vcc
	global_store_dwordx2 v[42:43], v[90:91], off offset:-4096 sc1
	v_mov_b32_e32 v90, v120
	v_mov_b32_e32 v91, v118
	v_mov_b32_e32 v118, v121
	v_pk_add_f32 v[90:91], v[90:91], v[118:119]
	v_mov_b32_e32 v71, s9
	v_pk_fma_f32 v[90:91], v[90:91], s[0:1], v[96:97] op_sel_hi:[1,0,0]
	v_pk_add_f32 v[68:69], s[2:3], v[68:69]
	v_mul_f32_e32 v89, 0x4b800000, v91
	v_cmp_gt_f32_e32 vcc, s1, v91
	v_pk_add_f32 v[70:71], s[4:5], v[70:71]
	s_nop 0
	v_cndmask_b32_e32 v89, v91, v89, vcc
	v_rsq_f32_e32 v91, v89
	v_cvt_f32_f16_sdwa v89, v32 dst_sel:DWORD dst_unused:UNUSED_PAD src0_sel:WORD_1
	v_cvt_f32_f16_e32 v32, v33
	v_cvt_f32_f16_sdwa v33, v33 dst_sel:DWORD dst_unused:UNUSED_PAD src0_sel:WORD_1
	v_mul_f32_e32 v92, 0x45800000, v91
	v_cndmask_b32_e32 v92, v91, v92, vcc
	v_pk_mul_f32 v[86:87], v[92:93], v[86:87] op_sel_hi:[0,1]
	v_pk_fma_f32 v[86:87], v[0:1], v[86:87], v[4:5]
	v_cmp_gt_f32_e32 vcc, s1, v90
	v_pk_mul_f32 v[86:87], v[86:87], v[88:89]
	v_pk_mul_f32 v[84:85], v[92:93], v[84:85] op_sel_hi:[0,1]
	v_cvt_pk_f16_f32 v86, v86, v87
	v_mul_f32_e32 v87, 0x4b800000, v90
	v_cndmask_b32_e32 v87, v90, v87, vcc
	v_rsq_f32_e32 v88, v87
	v_pk_fma_f32 v[84:85], v[2:3], v[84:85], v[6:7]
	s_nop 0
	v_pk_mul_f32 v[32:33], v[84:85], v[32:33]
	s_nop 0
	v_cvt_pk_f16_f32 v87, v32, v33
	global_store_dwordx2 v[42:43], v[86:87], off sc1
	v_mul_f32_e32 v42, 0x45800000, v88
	v_cvt_f32_f16_e32 v32, v28
	v_cvt_f32_f16_sdwa v33, v28 dst_sel:DWORD dst_unused:UNUSED_PAD src0_sel:WORD_1
	v_cndmask_b32_e32 v28, v88, v42, vcc
	v_pk_mul_f32 v[42:43], v[28:29], v[82:83] op_sel_hi:[0,1]
	v_pk_fma_f32 v[42:43], v[0:1], v[42:43], v[4:5]
	s_nop 0
	v_pk_mul_f32 v[32:33], v[42:43], v[32:33]
	v_cvt_f32_f16_e32 v42, v29
	v_cvt_f32_f16_sdwa v43, v29 dst_sel:DWORD dst_unused:UNUSED_PAD src0_sel:WORD_1
	v_pk_mul_f32 v[28:29], v[28:29], v[80:81] op_sel_hi:[0,1]
	v_pk_fma_f32 v[28:29], v[2:3], v[28:29], v[6:7]
	v_cvt_pk_f16_f32 v32, v32, v33
	v_pk_mul_f32 v[28:29], v[28:29], v[42:43]
	v_mov_b32_e32 v42, v116
	v_mov_b32_e32 v43, v114
	v_mov_b32_e32 v114, v117
	v_cvt_pk_f16_f32 v33, v28, v29
	v_add_co_u32_e32 v28, vcc, s16, v60
	v_pk_add_f32 v[42:43], v[42:43], v[114:115]
	s_nop 0
	v_addc_co_u32_e32 v29, vcc, 0, v61, vcc
	v_pk_fma_f32 v[42:43], v[42:43], s[0:1], v[96:97] op_sel_hi:[1,0,0]
	global_store_dwordx2 v[28:29], v[32:33], off offset:-4096 sc1
	v_mul_f32_e32 v33, 0x4b800000, v43
	v_cmp_gt_f32_e32 vcc, s1, v43
	v_cvt_f32_f16_e32 v32, v26
	s_nop 0
	v_cndmask_b32_e32 v33, v43, v33, vcc
	v_rsq_f32_e32 v43, v33
	v_cvt_f32_f16_sdwa v33, v26 dst_sel:DWORD dst_unused:UNUSED_PAD src0_sel:WORD_1
	v_cvt_f32_f16_e32 v26, v27
	v_cvt_f32_f16_sdwa v27, v27 dst_sel:DWORD dst_unused:UNUSED_PAD src0_sel:WORD_1
	v_mul_f32_e32 v80, 0x45800000, v43
	v_cndmask_b32_e32 v80, v43, v80, vcc
	v_pk_mul_f32 v[76:77], v[80:81], v[76:77] op_sel_hi:[0,1]
	v_pk_fma_f32 v[76:77], v[0:1], v[76:77], v[4:5]
	v_cmp_gt_f32_e32 vcc, s1, v42
	v_pk_mul_f32 v[32:33], v[76:77], v[32:33]
	v_pk_mul_f32 v[74:75], v[80:81], v[74:75] op_sel_hi:[0,1]
	v_cvt_pk_f16_f32 v32, v32, v33
	v_mul_f32_e32 v33, 0x4b800000, v42
	v_cndmask_b32_e32 v33, v42, v33, vcc
	v_rsq_f32_e32 v42, v33
	v_pk_fma_f32 v[74:75], v[2:3], v[74:75], v[6:7]
	s_nop 0
	v_pk_mul_f32 v[26:27], v[74:75], v[26:27]
	s_nop 0
	v_cvt_pk_f16_f32 v33, v26, v27
	global_store_dwordx2 v[28:29], v[32:33], off sc1
	v_mul_f32_e32 v28, 0x45800000, v42
	v_cvt_f32_f16_e32 v26, v24
	v_cvt_f32_f16_sdwa v27, v24 dst_sel:DWORD dst_unused:UNUSED_PAD src0_sel:WORD_1
	v_cndmask_b32_e32 v24, v42, v28, vcc
	v_pk_mul_f32 v[28:29], v[24:25], v[78:79] op_sel_hi:[0,1]
	v_pk_fma_f32 v[28:29], v[0:1], v[28:29], v[4:5]
	s_nop 0
	v_pk_mul_f32 v[26:27], v[28:29], v[26:27]
	v_cvt_f32_f16_e32 v28, v25
	v_cvt_f32_f16_sdwa v29, v25 dst_sel:DWORD dst_unused:UNUSED_PAD src0_sel:WORD_1
	v_pk_mul_f32 v[24:25], v[24:25], v[72:73] op_sel_hi:[0,1]
	v_pk_fma_f32 v[24:25], v[2:3], v[24:25], v[6:7]
	v_cvt_pk_f16_f32 v26, v26, v27
	v_pk_mul_f32 v[24:25], v[24:25], v[28:29]
	v_mov_b32_e32 v28, v110
	v_mov_b32_e32 v29, v108
	v_mov_b32_e32 v108, v111
	v_cvt_pk_f16_f32 v27, v24, v25
	v_add_co_u32_e32 v24, vcc, s15, v60
	v_pk_add_f32 v[28:29], v[28:29], v[108:109]
	s_nop 0
	v_addc_co_u32_e32 v25, vcc, 0, v61, vcc
	v_pk_fma_f32 v[28:29], v[28:29], s[0:1], v[96:97] op_sel_hi:[1,0,0]
	global_store_dwordx2 v[24:25], v[26:27], off offset:-4096 sc1
	v_mul_f32_e32 v27, 0x4b800000, v29
	v_cmp_gt_f32_e32 vcc, s1, v29
	v_cvt_f32_f16_e32 v26, v22
	s_nop 0
	v_cndmask_b32_e32 v27, v29, v27, vcc
	v_rsq_f32_e32 v29, v27
	v_cvt_f32_f16_sdwa v27, v22 dst_sel:DWORD dst_unused:UNUSED_PAD src0_sel:WORD_1
	v_cvt_f32_f16_e32 v22, v23
	v_cvt_f32_f16_sdwa v23, v23 dst_sel:DWORD dst_unused:UNUSED_PAD src0_sel:WORD_1
	v_mul_f32_e32 v32, 0x45800000, v29
	v_cndmask_b32_e32 v32, v29, v32, vcc
	v_pk_mul_f32 v[42:43], v[32:33], v[66:67] op_sel_hi:[0,1]
	v_pk_fma_f32 v[42:43], v[0:1], v[42:43], v[4:5]
	v_cmp_gt_f32_e32 vcc, s1, v28
	v_pk_mul_f32 v[26:27], v[42:43], v[26:27]
	v_pk_mul_f32 v[32:33], v[32:33], v[64:65] op_sel_hi:[0,1]
	v_cvt_pk_f16_f32 v26, v26, v27
	v_mul_f32_e32 v27, 0x4b800000, v28
	v_cndmask_b32_e32 v27, v28, v27, vcc
	v_rsq_f32_e32 v28, v27
	v_pk_fma_f32 v[32:33], v[2:3], v[32:33], v[6:7]
	s_nop 0
	v_pk_mul_f32 v[22:23], v[32:33], v[22:23]
	s_nop 0
	v_cvt_pk_f16_f32 v27, v22, v23
	global_store_dwordx2 v[24:25], v[26:27], off sc1
	v_mul_f32_e32 v24, 0x45800000, v28
	v_cvt_f32_f16_e32 v22, v20
	v_cvt_f32_f16_sdwa v23, v20 dst_sel:DWORD dst_unused:UNUSED_PAD src0_sel:WORD_1
	v_cndmask_b32_e32 v20, v28, v24, vcc
	v_pk_mul_f32 v[24:25], v[20:21], v[62:63] op_sel_hi:[0,1]
	v_pk_fma_f32 v[24:25], v[0:1], v[24:25], v[4:5]
	s_nop 0
	v_pk_mul_f32 v[22:23], v[24:25], v[22:23]
	v_cvt_f32_f16_e32 v24, v21
	v_cvt_f32_f16_sdwa v25, v21 dst_sel:DWORD dst_unused:UNUSED_PAD src0_sel:WORD_1
	v_pk_mul_f32 v[20:21], v[20:21], v[58:59] op_sel_hi:[0,1]
	v_pk_fma_f32 v[20:21], v[2:3], v[20:21], v[6:7]
	v_cvt_pk_f16_f32 v22, v22, v23
	v_pk_mul_f32 v[20:21], v[20:21], v[24:25]
	v_mov_b32_e32 v24, v104
	v_mov_b32_e32 v25, v102
	v_mov_b32_e32 v102, v105
	v_cvt_pk_f16_f32 v23, v20, v21
	v_add_co_u32_e32 v20, vcc, s14, v60
	v_pk_add_f32 v[24:25], v[24:25], v[102:103]
	s_nop 0
	v_addc_co_u32_e32 v21, vcc, 0, v61, vcc
	v_pk_fma_f32 v[24:25], v[24:25], s[0:1], v[96:97] op_sel_hi:[1,0,0]
	global_store_dwordx2 v[20:21], v[22:23], off offset:-4096 sc1
	v_mul_f32_e32 v23, 0x4b800000, v25
	v_cmp_gt_f32_e32 vcc, s1, v25
	v_cvt_f32_f16_e32 v22, v18
	s_nop 0
	v_cndmask_b32_e32 v23, v25, v23, vcc
	v_rsq_f32_e32 v25, v23
	v_cvt_f32_f16_sdwa v23, v18 dst_sel:DWORD dst_unused:UNUSED_PAD src0_sel:WORD_1
	v_cvt_f32_f16_e32 v18, v19
	v_cvt_f32_f16_sdwa v19, v19 dst_sel:DWORD dst_unused:UNUSED_PAD src0_sel:WORD_1
	v_mul_f32_e32 v26, 0x45800000, v25
	v_cndmask_b32_e32 v26, v25, v26, vcc
	v_pk_mul_f32 v[28:29], v[26:27], v[54:55] op_sel_hi:[0,1]
	v_pk_fma_f32 v[28:29], v[0:1], v[28:29], v[4:5]
	v_cmp_gt_f32_e32 vcc, s1, v24
	v_pk_mul_f32 v[22:23], v[28:29], v[22:23]
	v_pk_mul_f32 v[26:27], v[26:27], v[52:53] op_sel_hi:[0,1]
	v_cvt_pk_f16_f32 v22, v22, v23
	v_mul_f32_e32 v23, 0x4b800000, v24
	v_cndmask_b32_e32 v23, v24, v23, vcc
	v_rsq_f32_e32 v24, v23
	v_pk_fma_f32 v[26:27], v[2:3], v[26:27], v[6:7]
	s_nop 0
	v_pk_mul_f32 v[18:19], v[26:27], v[18:19]
	s_nop 0
	v_cvt_pk_f16_f32 v23, v18, v19
	global_store_dwordx2 v[20:21], v[22:23], off sc1
	v_mul_f32_e32 v20, 0x45800000, v24
	v_cvt_f32_f16_e32 v18, v16
	v_cvt_f32_f16_sdwa v19, v16 dst_sel:DWORD dst_unused:UNUSED_PAD src0_sel:WORD_1
	v_cndmask_b32_e32 v16, v24, v20, vcc
	v_pk_mul_f32 v[20:21], v[16:17], v[56:57] op_sel_hi:[0,1]
	v_pk_fma_f32 v[20:21], v[0:1], v[20:21], v[4:5]
	s_nop 0
	v_pk_mul_f32 v[18:19], v[20:21], v[18:19]
	v_cvt_f32_f16_e32 v20, v17
	v_cvt_f32_f16_sdwa v21, v17 dst_sel:DWORD dst_unused:UNUSED_PAD src0_sel:WORD_1
	v_pk_mul_f32 v[16:17], v[16:17], v[50:51] op_sel_hi:[0,1]
	v_pk_fma_f32 v[16:17], v[2:3], v[16:17], v[6:7]
	v_cvt_pk_f16_f32 v18, v18, v19
	v_pk_mul_f32 v[16:17], v[16:17], v[20:21]
	v_mov_b32_e32 v20, v100
	v_mov_b32_e32 v21, v98
	v_mov_b32_e32 v98, v101
	v_cvt_pk_f16_f32 v19, v16, v17
	v_add_co_u32_e32 v16, vcc, s13, v60
	v_pk_add_f32 v[20:21], v[20:21], v[98:99]
	s_nop 0
	v_addc_co_u32_e32 v17, vcc, 0, v61, vcc
	v_pk_fma_f32 v[20:21], v[20:21], s[0:1], v[96:97] op_sel_hi:[1,0,0]
	global_store_dwordx2 v[16:17], v[18:19], off offset:-4096 sc1
	v_mul_f32_e32 v19, 0x4b800000, v21
	v_cmp_gt_f32_e32 vcc, s1, v21
	v_cvt_f32_f16_e32 v18, v14
	s_nop 0
	v_cndmask_b32_e32 v19, v21, v19, vcc
	v_rsq_f32_e32 v21, v19
	v_cvt_f32_f16_sdwa v19, v14 dst_sel:DWORD dst_unused:UNUSED_PAD src0_sel:WORD_1
	v_cvt_f32_f16_e32 v14, v15
	v_cvt_f32_f16_sdwa v15, v15 dst_sel:DWORD dst_unused:UNUSED_PAD src0_sel:WORD_1
	v_mul_f32_e32 v22, 0x45800000, v21
	v_cndmask_b32_e32 v22, v21, v22, vcc
	v_pk_mul_f32 v[24:25], v[22:23], v[48:49] op_sel_hi:[0,1]
	v_pk_fma_f32 v[24:25], v[0:1], v[24:25], v[4:5]
	v_cmp_gt_f32_e32 vcc, s1, v20
	v_pk_mul_f32 v[18:19], v[24:25], v[18:19]
	v_pk_mul_f32 v[22:23], v[22:23], v[46:47] op_sel_hi:[0,1]
	v_cvt_pk_f16_f32 v18, v18, v19
	v_mul_f32_e32 v19, 0x4b800000, v20
	v_cndmask_b32_e32 v19, v20, v19, vcc
	v_rsq_f32_e32 v20, v19
	v_pk_fma_f32 v[22:23], v[2:3], v[22:23], v[6:7]
	s_nop 0
	v_pk_mul_f32 v[14:15], v[22:23], v[14:15]
	s_nop 0
	v_cvt_pk_f16_f32 v19, v14, v15
	global_store_dwordx2 v[16:17], v[18:19], off sc1
	v_mul_f32_e32 v16, 0x45800000, v20
	v_cvt_f32_f16_e32 v14, v12
	v_cvt_f32_f16_sdwa v15, v12 dst_sel:DWORD dst_unused:UNUSED_PAD src0_sel:WORD_1
	v_cndmask_b32_e32 v12, v20, v16, vcc
	v_pk_mul_f32 v[16:17], v[12:13], v[44:45] op_sel_hi:[0,1]
	v_pk_fma_f32 v[16:17], v[0:1], v[16:17], v[4:5]
	s_nop 0
	v_pk_mul_f32 v[14:15], v[16:17], v[14:15]
	v_cvt_f32_f16_e32 v16, v13
	v_cvt_f32_f16_sdwa v17, v13 dst_sel:DWORD dst_unused:UNUSED_PAD src0_sel:WORD_1
	v_pk_mul_f32 v[12:13], v[12:13], v[40:41] op_sel_hi:[0,1]
	v_pk_fma_f32 v[12:13], v[2:3], v[12:13], v[6:7]
	v_cvt_pk_f16_f32 v14, v14, v15
	v_pk_mul_f32 v[12:13], v[12:13], v[16:17]
	v_mov_b32_e32 v16, v70
	v_mov_b32_e32 v17, v68
	v_mov_b32_e32 v68, v71
	v_cvt_pk_f16_f32 v15, v12, v13
	v_add_co_u32_e32 v12, vcc, s12, v60
	v_pk_add_f32 v[16:17], v[16:17], v[68:69]
	s_nop 0
	v_addc_co_u32_e32 v13, vcc, 0, v61, vcc
	v_pk_fma_f32 v[16:17], v[16:17], s[0:1], v[96:97] op_sel_hi:[1,0,0]
	global_store_dwordx2 v[12:13], v[14:15], off offset:-4096 sc1
	v_mul_f32_e32 v15, 0x4b800000, v17
	v_cmp_gt_f32_e32 vcc, s1, v17
	v_cvt_f32_f16_e32 v14, v10
	s_nop 0
	v_cndmask_b32_e32 v15, v17, v15, vcc
	v_rsq_f32_e32 v17, v15
	v_cvt_f32_f16_sdwa v15, v10 dst_sel:DWORD dst_unused:UNUSED_PAD src0_sel:WORD_1
	v_cvt_f32_f16_e32 v10, v11
	v_cvt_f32_f16_sdwa v11, v11 dst_sel:DWORD dst_unused:UNUSED_PAD src0_sel:WORD_1
	v_mul_f32_e32 v18, 0x45800000, v17
	v_cndmask_b32_e32 v18, v17, v18, vcc
	v_pk_mul_f32 v[20:21], v[18:19], v[38:39] op_sel_hi:[0,1]
	v_pk_fma_f32 v[20:21], v[0:1], v[20:21], v[4:5]
	v_cmp_gt_f32_e32 vcc, s1, v16
	v_pk_mul_f32 v[14:15], v[20:21], v[14:15]
	v_pk_mul_f32 v[18:19], v[18:19], v[36:37] op_sel_hi:[0,1]
	v_cvt_pk_f16_f32 v14, v14, v15
	v_mul_f32_e32 v15, 0x4b800000, v16
	v_cndmask_b32_e32 v15, v16, v15, vcc
	v_rsq_f32_e32 v16, v15
	v_pk_fma_f32 v[18:19], v[2:3], v[18:19], v[6:7]
	s_nop 0
	v_pk_mul_f32 v[10:11], v[18:19], v[10:11]
	s_nop 0
	v_cvt_pk_f16_f32 v15, v10, v11
	global_store_dwordx2 v[12:13], v[14:15], off sc1
	v_mul_f32_e32 v12, 0x45800000, v16
	v_cvt_f32_f16_e32 v10, v8
	v_cvt_f32_f16_sdwa v11, v8 dst_sel:DWORD dst_unused:UNUSED_PAD src0_sel:WORD_1
	v_cndmask_b32_e32 v8, v16, v12, vcc
	v_pk_mul_f32 v[12:13], v[8:9], v[34:35] op_sel_hi:[0,1]
	v_pk_fma_f32 v[0:1], v[0:1], v[12:13], v[4:5]
	v_cvt_f32_f16_e32 v4, v9
	v_cvt_f32_f16_sdwa v5, v9 dst_sel:DWORD dst_unused:UNUSED_PAD src0_sel:WORD_1
	v_pk_mul_f32 v[8:9], v[8:9], v[30:31] op_sel_hi:[0,1]
	v_pk_fma_f32 v[2:3], v[2:3], v[8:9], v[6:7]
	v_pk_mul_f32 v[0:1], v[0:1], v[10:11]
	v_pk_mul_f32 v[2:3], v[2:3], v[4:5]
	v_cvt_pk_f16_f32 v0, v0, v1
	v_cvt_pk_f16_f32 v1, v2, v3
	v_add_co_u32_e32 v2, vcc, 0xf000, v60
	s_nop 1
	v_addc_co_u32_e32 v3, vcc, 0, v61, vcc
	global_store_dwordx2 v[2:3], v[0:1], off sc1
	s_endpgm
	.p2align	8
